# speedup vs baseline: 1.2613x; 1.2613x over previous
.LBB2_13:
	s_or_b64 exec, exec, s[12:13]
	s_waitcnt vmcnt(0)
	v_cmp_lt_i32_e64 s[0:1], -1, v8
	v_mov_b32_e32 v16, 0
	v_mov_b32_e32 v18, 0
	v_mov_b32_e32 v19, 0
	s_and_saveexec_b64 s[12:13], s[0:1]
	s_cbranch_execz .LBB2_15
	v_lshl_add_u64 v[18:19], v[8:9], 3, s[2:3]
	global_load_dwordx2 v[18:19], v[18:19], off sc1
.LBB2_15:
	s_or_b64 exec, exec, s[12:13]
	v_cmp_lt_i32_e64 s[0:1], -1, v14
	v_mov_b32_e32 v17, 0
	s_and_saveexec_b64 s[12:13], s[0:1]
	s_cbranch_execz .LBB2_17
	v_mov_b32_e32 v15, v9
	v_lshl_add_u64 v[14:15], v[14:15], 3, s[2:3]
	global_load_dwordx2 v[16:17], v[14:15], off sc1
.LBB2_17:
	s_or_b64 exec, exec, s[12:13]
	v_cmp_lt_i32_e64 s[0:1], -1, v20
	v_mov_b32_e32 v14, 0
	v_mov_b32_e32 v22, 0
	v_mov_b32_e32 v23, 0
	s_and_saveexec_b64 s[12:13], s[0:1]
	s_cbranch_execz .LBB2_19
	v_mov_b32_e32 v21, v9
	v_lshl_add_u64 v[20:21], v[20:21], 3, s[2:3]
	global_load_dwordx2 v[22:23], v[20:21], off sc1
.LBB2_19:
	s_or_b64 exec, exec, s[12:13]
	v_cmp_lt_i32_e64 s[0:1], -1, v12
	v_mov_b32_e32 v15, 0
	s_and_saveexec_b64 s[12:13], s[0:1]
	s_cbranch_execz .LBB2_4
	v_mov_b32_e32 v13, v9
	v_lshl_add_u64 v[12:13], v[12:13], 3, s[2:3]
	global_load_dwordx2 v[14:15], v[12:13], off sc1
	s_branch .LBB2_4
